# pipelined attention: first 8 softmax VALU ops of a block issued in the post-barrier LDS latency window
# speedup vs baseline: 1.0059x; 1.0059x over previous
.LBB0_734:
	s_waitcnt lgkmcnt(0)
	s_barrier
	ds_read_b128 v[160:163], v201 offset:16384
	ds_read_b128 v[164:167], v209 offset:0
	ds_read_b128 v[168:171], v202 offset:16384
	ds_read_b128 v[172:175], v209 offset:2048
	ds_read_b128 v[176:179], v203 offset:16384
	ds_read_b128 v[180:183], v209 offset:4096
	ds_read_b128 v[230:233], v246 offset:16384
	v_exp_f32_e32 v88, v88
	v_exp_f32_e32 v92, v92
	v_cvt_pk_bf16_f32 v242, v80, v81
	v_exp_f32_e32 v89, v89
	v_exp_f32_e32 v93, v93
	v_cvt_pk_bf16_f32 v243, v82, v83
	v_exp_f32_e32 v90, v90
	v_exp_f32_e32 v94, v94
	s_waitcnt lgkmcnt(6)
	v_mfma_f32_16x16x32_bf16 v[64:67], v[160:163], v[96:99], 0
	v_cvt_pk_bf16_f32 v204, v84, v85
	v_mfma_f32_16x16x32_bf16 v[68:71], v[160:163], v[112:115], 0
	v_exp_f32_e32 v91, v91
	ds_read_b128 v[234:237], v209 offset:6144
	s_add_u32 s16, s22, s10
	s_addc_u32 s17, s23, s11
	s_add_u32 s15, s22, s12
	s_addc_u32 s14, s23, s13
	s_add_u32 s8, s16, 0x3bc00200
	s_addc_u32 s9, s17, 0
	s_add_u32 s6, s15, 0x23a50000
	s_addc_u32 s7, s14, 0
	s_waitcnt lgkmcnt(6)
	v_mfma_f32_16x16x32_bf16 v[0:3], v[164:167], v[216:219], v[0:3]
	v_exp_f32_e32 v95, v95
	v_mfma_f32_16x16x32_bf16 v[4:7], v[164:167], v[238:241], v[4:7]
	v_cvt_pk_bf16_f32 v205, v86, v87
	ds_read_b128 v[160:163], v201 offset:20480
	s_waitcnt vmcnt(4)
	ds_write_b128 v225, v[152:155] offset:49152
	s_waitcnt lgkmcnt(7)
	v_mfma_f32_16x16x32_bf16 v[68:71], v[168:171], v[116:119], v[68:71]
	v_add_f32_e32 v220, v220, v88
	v_mfma_f32_16x16x32_bf16 v[64:67], v[168:171], v[100:103], v[64:67]
	v_add_f32_e32 v221, v221, v92
	ds_read_b128 v[164:167], v209 offset:8192
	ds_write_b128 v226, v[156:159] offset:49152
	s_waitcnt lgkmcnt(8)
	v_mfma_f32_16x16x32_bf16 v[12:15], v[172:175], v[238:241], v[12:15]
	v_add_f32_e32 v220, v220, v89
	v_mfma_f32_16x16x32_bf16 v[8:11], v[172:175], v[216:219], v[8:11]
	v_add_f32_e32 v221, v221, v93
	ds_read_b128 v[168:171], v202 offset:20480
	ds_write_b64 v227, v[132:133] offset:32768
	s_waitcnt lgkmcnt(9)
	v_mfma_f32_16x16x32_bf16 v[64:67], v[176:179], v[104:107], v[64:67]
	v_cvt_pk_bf16_f32 v244, v88, v89
	v_mfma_f32_16x16x32_bf16 v[68:71], v[176:179], v[120:123], v[68:71]
	v_cvt_pk_bf16_f32 v245, v90, v91
	ds_read_b128 v[172:175], v209 offset:10240
	ds_write_b64 v228, v[134:135] offset:32768
	s_waitcnt lgkmcnt(10)
	v_mfma_f32_16x16x32_bf16 v[16:19], v[180:183], v[216:219], v[16:19]
	v_cvt_pk_bf16_f32 v206, v92, v93
	v_mfma_f32_16x16x32_bf16 v[20:23], v[180:183], v[238:241], v[20:23]
	v_cvt_pk_bf16_f32 v207, v94, v95
	ds_read_b128 v[176:179], v203 offset:20480
	ds_write_b64 v229, v[128:129] offset:32768
	s_waitcnt lgkmcnt(11)
	v_mfma_f32_16x16x32_bf16 v[68:71], v[230:233], v[124:127], v[68:71]
	v_mfma_f32_16x16x32_bf16 v[64:67], v[230:233], v[108:111], v[64:67]
	ds_read_b128 v[180:183], v209 offset:12288
	ds_write_b64 v184, v[130:131] offset:32768
	s_waitcnt lgkmcnt(12)
	v_mfma_f32_16x16x32_bf16 v[28:31], v[234:237], v[238:241], v[28:31]
	v_mfma_f32_16x16x32_bf16 v[24:27], v[234:237], v[216:219], v[24:27]
	ds_read_b128 v[230:233], v246 offset:20480
	global_load_dwordx4 v[132:135], v198, s[8:9]
	s_waitcnt lgkmcnt(12)
	v_mfma_f32_16x16x32_bf16 v[72:75], v[160:163], v[96:99], 0
	v_add_f32_e32 v220, v220, v90
	v_add_f32_e32 v221, v221, v94
	v_mfma_f32_16x16x32_bf16 v[76:79], v[160:163], v[112:115], 0
	v_add_f32_e32 v220, v220, v91
	v_add_f32_e32 v221, v221, v95
	ds_read_b128 v[234:237], v209 offset:14336
	global_load_dwordx4 v[128:131], v199, s[8:9]
	s_waitcnt lgkmcnt(11)
	v_mfma_f32_16x16x32_bf16 v[32:35], v[164:167], v[216:219], v[32:35]
	v_add_f32_e32 v194, v194, v220
	v_add_f32_e32 v195, v195, v221
	v_mfma_f32_16x16x32_bf16 v[36:39], v[164:167], v[238:241], v[36:39]
	v_exp_f32_e32 v64, v64
	v_exp_f32_e32 v68, v68
	ds_read_b128 v[160:163], v201 offset:24576
	global_load_dwordx4 v[152:155], v196, s[6:7]
	s_waitcnt lgkmcnt(10)
	v_mfma_f32_16x16x32_bf16 v[76:79], v[168:171], v[116:119], v[76:79]
	v_exp_f32_e32 v65, v65
	v_mfma_f32_16x16x32_bf16 v[72:75], v[168:171], v[100:103], v[72:75]
	v_exp_f32_e32 v69, v69
	ds_read_b128 v[164:167], v210 offset:0
	global_load_dwordx4 v[156:159], v197, s[6:7]
	s_waitcnt lgkmcnt(9)
	v_mfma_f32_16x16x32_bf16 v[44:47], v[172:175], v[238:241], v[44:47]
	v_exp_f32_e32 v66, v66
	v_mfma_f32_16x16x32_bf16 v[40:43], v[172:175], v[216:219], v[40:43]
	v_exp_f32_e32 v70, v70
	ds_read_b128 v[168:171], v202 offset:24576
	s_waitcnt lgkmcnt(8)
	v_mfma_f32_16x16x32_bf16 v[72:75], v[176:179], v[104:107], v[72:75]
	v_exp_f32_e32 v67, v67
	v_mfma_f32_16x16x32_bf16 v[76:79], v[176:179], v[120:123], v[76:79]
	v_exp_f32_e32 v71, v71
	ds_read_b128 v[172:175], v210 offset:2048
	s_waitcnt lgkmcnt(7)
	v_mfma_f32_16x16x32_bf16 v[48:51], v[180:183], v[216:219], v[48:51]
	v_add_f32_e32 v220, v64, v65
	v_mfma_f32_16x16x32_bf16 v[52:55], v[180:183], v[238:241], v[52:55]
	v_add_f32_e32 v221, v68, v69
	ds_read_b128 v[176:179], v203 offset:24576
	s_waitcnt lgkmcnt(6)
	v_mfma_f32_16x16x32_bf16 v[76:79], v[230:233], v[124:127], v[76:79]
	v_add_f32_e32 v220, v220, v66
	v_mfma_f32_16x16x32_bf16 v[72:75], v[230:233], v[108:111], v[72:75]
	v_add_f32_e32 v221, v221, v70
	ds_read_b128 v[180:183], v210 offset:4096
	s_waitcnt lgkmcnt(6)
	v_mfma_f32_16x16x32_bf16 v[60:63], v[234:237], v[238:241], v[60:63]
	v_add_f32_e32 v220, v220, v67
	v_mfma_f32_16x16x32_bf16 v[56:59], v[234:237], v[216:219], v[56:59]
	v_add_f32_e32 v221, v221, v71
	ds_read_b128 v[230:233], v246 offset:24576
	s_waitcnt lgkmcnt(6)
	v_mfma_f32_16x16x32_bf16 v[80:83], v[160:163], v[96:99], 0
	v_exp_f32_e32 v72, v72
	v_exp_f32_e32 v76, v76
	v_mfma_f32_16x16x32_bf16 v[84:87], v[160:163], v[112:115], 0
	v_exp_f32_e32 v73, v73
	v_exp_f32_e32 v77, v77
	ds_read_b128 v[234:237], v210 offset:6144
	s_waitcnt lgkmcnt(6)
	v_mfma_f32_16x16x32_bf16 v[0:3], v[164:167], v[242:245], v[0:3]
	v_exp_f32_e32 v74, v74
	v_exp_f32_e32 v78, v78
	v_mfma_f32_16x16x32_bf16 v[4:7], v[164:167], v[204:207], v[4:7]
	v_exp_f32_e32 v75, v75
	v_exp_f32_e32 v79, v79
	ds_read_b128 v[160:163], v201 offset:28672
	s_waitcnt lgkmcnt(6)
	v_mfma_f32_16x16x32_bf16 v[84:87], v[168:171], v[116:119], v[84:87]
	v_add_f32_e32 v220, v220, v72
	v_mfma_f32_16x16x32_bf16 v[80:83], v[168:171], v[100:103], v[80:83]
	v_add_f32_e32 v221, v221, v76
	ds_read_b128 v[164:167], v210 offset:8192
	s_waitcnt lgkmcnt(6)
	v_mfma_f32_16x16x32_bf16 v[12:15], v[172:175], v[204:207], v[12:15]
	v_add_f32_e32 v220, v220, v73
	v_mfma_f32_16x16x32_bf16 v[8:11], v[172:175], v[242:245], v[8:11]
	v_add_f32_e32 v221, v221, v77
	ds_read_b128 v[168:171], v202 offset:28672
	s_waitcnt lgkmcnt(6)
	v_mfma_f32_16x16x32_bf16 v[80:83], v[176:179], v[104:107], v[80:83]
	v_add_f32_e32 v220, v220, v74
	v_mfma_f32_16x16x32_bf16 v[84:87], v[176:179], v[120:123], v[84:87]
	v_add_f32_e32 v221, v221, v78
	ds_read_b128 v[172:175], v210 offset:10240
	s_waitcnt lgkmcnt(6)
	v_mfma_f32_16x16x32_bf16 v[16:19], v[180:183], v[242:245], v[16:19]
	v_add_f32_e32 v220, v220, v75
	v_mfma_f32_16x16x32_bf16 v[20:23], v[180:183], v[204:207], v[20:23]
	v_add_f32_e32 v221, v221, v79
	ds_read_b128 v[176:179], v203 offset:28672
	s_waitcnt lgkmcnt(6)
	v_mfma_f32_16x16x32_bf16 v[84:87], v[230:233], v[124:127], v[84:87]
	v_cvt_pk_bf16_f32 v216, v64, v65
	v_mfma_f32_16x16x32_bf16 v[80:83], v[230:233], v[108:111], v[80:83]
	v_cvt_pk_bf16_f32 v217, v66, v67
	ds_read_b128 v[180:183], v210 offset:12288
	s_waitcnt lgkmcnt(6)
	v_mfma_f32_16x16x32_bf16 v[28:31], v[234:237], v[204:207], v[28:31]
	v_cvt_pk_bf16_f32 v238, v68, v69
	v_mfma_f32_16x16x32_bf16 v[24:27], v[234:237], v[242:245], v[24:27]
	v_cvt_pk_bf16_f32 v239, v70, v71
	ds_read_b128 v[230:233], v246 offset:28672
	s_waitcnt lgkmcnt(6)
	v_mfma_f32_16x16x32_bf16 v[88:91], v[160:163], v[96:99], 0
	v_exp_f32_e32 v80, v80
	v_exp_f32_e32 v84, v84
	v_mfma_f32_16x16x32_bf16 v[92:95], v[160:163], v[112:115], 0
	v_exp_f32_e32 v81, v81
	v_exp_f32_e32 v85, v85
	ds_read_b128 v[234:237], v210 offset:14336
	s_waitcnt lgkmcnt(6)
	v_mfma_f32_16x16x32_bf16 v[32:35], v[164:167], v[242:245], v[32:35]
	v_exp_f32_e32 v82, v82
	v_exp_f32_e32 v86, v86
	v_mfma_f32_16x16x32_bf16 v[36:39], v[164:167], v[204:207], v[36:39]
	v_exp_f32_e32 v83, v83
	v_exp_f32_e32 v87, v87
	ds_read_b128 v[160:163], v201 offset:32768
	s_waitcnt lgkmcnt(6)
	v_mfma_f32_16x16x32_bf16 v[92:95], v[168:171], v[116:119], v[92:95]
	v_add_f32_e32 v220, v220, v80
	v_mfma_f32_16x16x32_bf16 v[88:91], v[168:171], v[100:103], v[88:91]
	v_add_f32_e32 v221, v221, v84
	ds_read_b128 v[164:167], v209 offset:16384
	s_waitcnt lgkmcnt(6)
	v_mfma_f32_16x16x32_bf16 v[44:47], v[172:175], v[204:207], v[44:47]
	v_add_f32_e32 v220, v220, v81
	v_mfma_f32_16x16x32_bf16 v[40:43], v[172:175], v[242:245], v[40:43]
	v_add_f32_e32 v221, v221, v85
	ds_read_b128 v[168:171], v202 offset:32768
	s_waitcnt lgkmcnt(6)
	v_mfma_f32_16x16x32_bf16 v[88:91], v[176:179], v[104:107], v[88:91]
	v_add_f32_e32 v220, v220, v82
	v_mfma_f32_16x16x32_bf16 v[92:95], v[176:179], v[120:123], v[92:95]
	v_add_f32_e32 v221, v221, v86
	ds_read_b128 v[172:175], v209 offset:18432
	s_waitcnt lgkmcnt(6)
	v_mfma_f32_16x16x32_bf16 v[48:51], v[180:183], v[242:245], v[48:51]
	v_add_f32_e32 v220, v220, v83
	v_mfma_f32_16x16x32_bf16 v[52:55], v[180:183], v[204:207], v[52:55]
	v_add_f32_e32 v221, v221, v87
	ds_read_b128 v[176:179], v203 offset:32768
	s_waitcnt lgkmcnt(6)
	v_mfma_f32_16x16x32_bf16 v[92:95], v[230:233], v[124:127], v[92:95]
	v_cvt_pk_bf16_f32 v218, v72, v73
	v_mfma_f32_16x16x32_bf16 v[88:91], v[230:233], v[108:111], v[88:91]
	v_cvt_pk_bf16_f32 v219, v74, v75
	ds_read_b128 v[180:183], v209 offset:20480
	s_waitcnt lgkmcnt(6)
	v_mfma_f32_16x16x32_bf16 v[60:63], v[234:237], v[204:207], v[60:63]
	v_cvt_pk_bf16_f32 v240, v76, v77
	v_mfma_f32_16x16x32_bf16 v[56:59], v[234:237], v[242:245], v[56:59]
	v_cvt_pk_bf16_f32 v241, v78, v79
	ds_read_b128 v[230:233], v246 offset:32768
	s_waitcnt lgkmcnt(6)
	v_mfma_f32_16x16x32_bf16 v[64:67], v[160:163], v[96:99], 0
	v_exp_f32_e32 v88, v88
	v_exp_f32_e32 v92, v92
	v_mfma_f32_16x16x32_bf16 v[68:71], v[160:163], v[112:115], 0
	v_cvt_pk_bf16_f32 v242, v80, v81
	v_exp_f32_e32 v89, v89
	ds_read_b128 v[234:237], v209 offset:22528
	s_add_u32 s8, s16, 0x3bc00280
	s_addc_u32 s9, s17, 0
	s_add_u32 s6, s15, 0x23a60000
	s_addc_u32 s7, s14, 0
	s_waitcnt lgkmcnt(6)
	v_mfma_f32_16x16x32_bf16 v[0:3], v[164:167], v[216:219], v[0:3]
	v_exp_f32_e32 v93, v93
	v_cvt_pk_bf16_f32 v243, v82, v83
	v_mfma_f32_16x16x32_bf16 v[4:7], v[164:167], v[238:241], v[4:7]
	v_exp_f32_e32 v90, v90
	v_exp_f32_e32 v94, v94
	ds_read_b128 v[160:163], v201 offset:36864
	s_waitcnt vmcnt(4)
	ds_write_b128 v225, v[136:139] offset:0
	s_waitcnt lgkmcnt(7)
	v_mfma_f32_16x16x32_bf16 v[68:71], v[168:171], v[116:119], v[68:71]
	v_cvt_pk_bf16_f32 v204, v84, v85
	v_mfma_f32_16x16x32_bf16 v[64:67], v[168:171], v[100:103], v[64:67]
	v_exp_f32_e32 v91, v91
	ds_read_b128 v[164:167], v209 offset:24576
	ds_write_b128 v226, v[140:143] offset:0
	s_waitcnt lgkmcnt(8)
	v_mfma_f32_16x16x32_bf16 v[12:15], v[172:175], v[238:241], v[12:15]
	v_exp_f32_e32 v95, v95
	v_mfma_f32_16x16x32_bf16 v[8:11], v[172:175], v[216:219], v[8:11]
	v_cvt_pk_bf16_f32 v205, v86, v87
	ds_read_b128 v[168:171], v202 offset:36864
	ds_write_b64 v227, v[148:149] offset:49152
	s_waitcnt lgkmcnt(9)
	v_mfma_f32_16x16x32_bf16 v[64:67], v[176:179], v[104:107], v[64:67]
	v_add_f32_e32 v220, v220, v88
	v_mfma_f32_16x16x32_bf16 v[68:71], v[176:179], v[120:123], v[68:71]
	v_add_f32_e32 v221, v221, v92
	ds_read_b128 v[172:175], v209 offset:26624
	ds_write_b64 v228, v[150:151] offset:49152
	s_waitcnt lgkmcnt(10)
	v_mfma_f32_16x16x32_bf16 v[16:19], v[180:183], v[216:219], v[16:19]
	v_add_f32_e32 v220, v220, v89
	v_mfma_f32_16x16x32_bf16 v[20:23], v[180:183], v[238:241], v[20:23]
	v_add_f32_e32 v221, v221, v93
	ds_read_b128 v[176:179], v203 offset:36864
	ds_write_b64 v229, v[144:145] offset:49152
	s_waitcnt lgkmcnt(11)
	v_mfma_f32_16x16x32_bf16 v[68:71], v[230:233], v[124:127], v[68:71]
	v_cvt_pk_bf16_f32 v244, v88, v89
	v_mfma_f32_16x16x32_bf16 v[64:67], v[230:233], v[108:111], v[64:67]
	v_cvt_pk_bf16_f32 v245, v90, v91
	ds_read_b128 v[180:183], v209 offset:28672
	ds_write_b64 v184, v[146:147] offset:49152
	s_waitcnt lgkmcnt(12)
	v_mfma_f32_16x16x32_bf16 v[28:31], v[234:237], v[238:241], v[28:31]
	v_cvt_pk_bf16_f32 v206, v92, v93
	v_mfma_f32_16x16x32_bf16 v[24:27], v[234:237], v[216:219], v[24:27]
	v_cvt_pk_bf16_f32 v207, v94, v95
	ds_read_b128 v[230:233], v246 offset:36864
	global_load_dwordx4 v[148:151], v198, s[8:9]
	s_waitcnt lgkmcnt(12)
	v_mfma_f32_16x16x32_bf16 v[72:75], v[160:163], v[96:99], 0
	v_add_f32_e32 v220, v220, v90
	v_add_f32_e32 v221, v221, v94
	v_mfma_f32_16x16x32_bf16 v[76:79], v[160:163], v[112:115], 0
	v_add_f32_e32 v220, v220, v91
	v_add_f32_e32 v221, v221, v95
	ds_read_b128 v[234:237], v209 offset:30720
	global_load_dwordx4 v[144:147], v199, s[8:9]
	s_waitcnt lgkmcnt(11)
	v_mfma_f32_16x16x32_bf16 v[32:35], v[164:167], v[216:219], v[32:35]
	v_add_f32_e32 v194, v194, v220
	v_add_f32_e32 v195, v195, v221
	v_mfma_f32_16x16x32_bf16 v[36:39], v[164:167], v[238:241], v[36:39]
	v_exp_f32_e32 v64, v64
	v_exp_f32_e32 v68, v68
	ds_read_b128 v[160:163], v201 offset:40960
	global_load_dwordx4 v[136:139], v196, s[6:7]
	s_waitcnt lgkmcnt(10)
	v_mfma_f32_16x16x32_bf16 v[76:79], v[168:171], v[116:119], v[76:79]
	v_exp_f32_e32 v65, v65
	v_mfma_f32_16x16x32_bf16 v[72:75], v[168:171], v[100:103], v[72:75]
	v_exp_f32_e32 v69, v69
	ds_read_b128 v[164:167], v210 offset:16384
	global_load_dwordx4 v[140:143], v197, s[6:7]
	s_waitcnt lgkmcnt(9)
	v_mfma_f32_16x16x32_bf16 v[44:47], v[172:175], v[238:241], v[44:47]
	v_exp_f32_e32 v66, v66
	v_mfma_f32_16x16x32_bf16 v[40:43], v[172:175], v[216:219], v[40:43]
	v_exp_f32_e32 v70, v70
	ds_read_b128 v[168:171], v202 offset:40960
	s_waitcnt lgkmcnt(8)
	v_mfma_f32_16x16x32_bf16 v[72:75], v[176:179], v[104:107], v[72:75]
	v_exp_f32_e32 v67, v67
	v_mfma_f32_16x16x32_bf16 v[76:79], v[176:179], v[120:123], v[76:79]
	v_exp_f32_e32 v71, v71
	ds_read_b128 v[172:175], v210 offset:18432
	s_waitcnt lgkmcnt(7)
	v_mfma_f32_16x16x32_bf16 v[48:51], v[180:183], v[216:219], v[48:51]
	v_add_f32_e32 v220, v64, v65
	v_mfma_f32_16x16x32_bf16 v[52:55], v[180:183], v[238:241], v[52:55]
	v_add_f32_e32 v221, v68, v69
	ds_read_b128 v[176:179], v203 offset:40960
	s_waitcnt lgkmcnt(6)
	v_mfma_f32_16x16x32_bf16 v[76:79], v[230:233], v[124:127], v[76:79]
	v_add_f32_e32 v220, v220, v66
	v_mfma_f32_16x16x32_bf16 v[72:75], v[230:233], v[108:111], v[72:75]
	v_add_f32_e32 v221, v221, v70
	ds_read_b128 v[180:183], v210 offset:20480
	s_waitcnt lgkmcnt(6)
	v_mfma_f32_16x16x32_bf16 v[60:63], v[234:237], v[238:241], v[60:63]
	v_add_f32_e32 v220, v220, v67
	v_mfma_f32_16x16x32_bf16 v[56:59], v[234:237], v[216:219], v[56:59]
	v_add_f32_e32 v221, v221, v71
	ds_read_b128 v[230:233], v246 offset:40960
	s_waitcnt lgkmcnt(6)
	v_mfma_f32_16x16x32_bf16 v[80:83], v[160:163], v[96:99], 0
	v_exp_f32_e32 v72, v72
	v_exp_f32_e32 v76, v76
	v_mfma_f32_16x16x32_bf16 v[84:87], v[160:163], v[112:115], 0
	v_exp_f32_e32 v73, v73
	v_exp_f32_e32 v77, v77
	ds_read_b128 v[234:237], v210 offset:22528
	s_waitcnt lgkmcnt(6)
	v_mfma_f32_16x16x32_bf16 v[0:3], v[164:167], v[242:245], v[0:3]
	v_exp_f32_e32 v74, v74
	v_exp_f32_e32 v78, v78
	v_mfma_f32_16x16x32_bf16 v[4:7], v[164:167], v[204:207], v[4:7]
	v_exp_f32_e32 v75, v75
	v_exp_f32_e32 v79, v79
	ds_read_b128 v[160:163], v201 offset:45056
	s_waitcnt lgkmcnt(6)
	v_mfma_f32_16x16x32_bf16 v[84:87], v[168:171], v[116:119], v[84:87]
	v_add_f32_e32 v220, v220, v72
	v_mfma_f32_16x16x32_bf16 v[80:83], v[168:171], v[100:103], v[80:83]
	v_add_f32_e32 v221, v221, v76
	ds_read_b128 v[164:167], v210 offset:24576
	s_waitcnt lgkmcnt(6)
	v_mfma_f32_16x16x32_bf16 v[12:15], v[172:175], v[204:207], v[12:15]
	v_add_f32_e32 v220, v220, v73
	v_mfma_f32_16x16x32_bf16 v[8:11], v[172:175], v[242:245], v[8:11]
	v_add_f32_e32 v221, v221, v77
	ds_read_b128 v[168:171], v202 offset:45056
	s_waitcnt lgkmcnt(6)
	v_mfma_f32_16x16x32_bf16 v[80:83], v[176:179], v[104:107], v[80:83]
	v_add_f32_e32 v220, v220, v74
	v_mfma_f32_16x16x32_bf16 v[84:87], v[176:179], v[120:123], v[84:87]
	v_add_f32_e32 v221, v221, v78
	ds_read_b128 v[172:175], v210 offset:26624
	s_waitcnt lgkmcnt(6)
	v_mfma_f32_16x16x32_bf16 v[16:19], v[180:183], v[242:245], v[16:19]
	v_add_f32_e32 v220, v220, v75
	v_mfma_f32_16x16x32_bf16 v[20:23], v[180:183], v[204:207], v[20:23]
	v_add_f32_e32 v221, v221, v79
	ds_read_b128 v[176:179], v203 offset:45056
	s_waitcnt lgkmcnt(6)
	v_mfma_f32_16x16x32_bf16 v[84:87], v[230:233], v[124:127], v[84:87]
	v_cvt_pk_bf16_f32 v216, v64, v65
	v_mfma_f32_16x16x32_bf16 v[80:83], v[230:233], v[108:111], v[80:83]
	v_cvt_pk_bf16_f32 v217, v66, v67
	ds_read_b128 v[180:183], v210 offset:28672
	s_waitcnt lgkmcnt(6)
	v_mfma_f32_16x16x32_bf16 v[28:31], v[234:237], v[204:207], v[28:31]
	v_cvt_pk_bf16_f32 v238, v68, v69
	v_mfma_f32_16x16x32_bf16 v[24:27], v[234:237], v[242:245], v[24:27]
	v_cvt_pk_bf16_f32 v239, v70, v71
	ds_read_b128 v[230:233], v246 offset:45056
	s_waitcnt lgkmcnt(6)
	v_mfma_f32_16x16x32_bf16 v[88:91], v[160:163], v[96:99], 0
	v_exp_f32_e32 v80, v80
	v_exp_f32_e32 v84, v84
	v_mfma_f32_16x16x32_bf16 v[92:95], v[160:163], v[112:115], 0
	v_exp_f32_e32 v81, v81
	v_exp_f32_e32 v85, v85
	ds_read_b128 v[234:237], v210 offset:30720
	s_waitcnt lgkmcnt(6)
	v_mfma_f32_16x16x32_bf16 v[32:35], v[164:167], v[242:245], v[32:35]
	v_exp_f32_e32 v82, v82
	v_exp_f32_e32 v86, v86
	v_mfma_f32_16x16x32_bf16 v[36:39], v[164:167], v[204:207], v[36:39]
	v_exp_f32_e32 v83, v83
	v_exp_f32_e32 v87, v87
	s_waitcnt lgkmcnt(5)
	v_mfma_f32_16x16x32_bf16 v[92:95], v[168:171], v[116:119], v[92:95]
	v_add_f32_e32 v220, v220, v80
	v_mfma_f32_16x16x32_bf16 v[88:91], v[168:171], v[100:103], v[88:91]
	v_add_f32_e32 v221, v221, v84
	s_waitcnt lgkmcnt(4)
	v_mfma_f32_16x16x32_bf16 v[44:47], v[172:175], v[204:207], v[44:47]
	v_add_f32_e32 v220, v220, v81
	v_mfma_f32_16x16x32_bf16 v[40:43], v[172:175], v[242:245], v[40:43]
	v_add_f32_e32 v221, v221, v85
	s_waitcnt lgkmcnt(3)
	v_mfma_f32_16x16x32_bf16 v[88:91], v[176:179], v[104:107], v[88:91]
	v_add_f32_e32 v220, v220, v82
	v_mfma_f32_16x16x32_bf16 v[92:95], v[176:179], v[120:123], v[92:95]
	v_add_f32_e32 v221, v221, v86
	s_waitcnt lgkmcnt(2)
	v_mfma_f32_16x16x32_bf16 v[48:51], v[180:183], v[242:245], v[48:51]
	v_add_f32_e32 v220, v220, v83
	v_mfma_f32_16x16x32_bf16 v[52:55], v[180:183], v[204:207], v[52:55]
	v_add_f32_e32 v221, v221, v87
	s_waitcnt lgkmcnt(1)
	v_mfma_f32_16x16x32_bf16 v[92:95], v[230:233], v[124:127], v[92:95]
	v_cvt_pk_bf16_f32 v218, v72, v73
	v_mfma_f32_16x16x32_bf16 v[88:91], v[230:233], v[108:111], v[88:91]
	v_cvt_pk_bf16_f32 v219, v74, v75
	s_waitcnt lgkmcnt(0)
	v_mfma_f32_16x16x32_bf16 v[60:63], v[234:237], v[204:207], v[60:63]
	v_cvt_pk_bf16_f32 v240, v76, v77
	v_mfma_f32_16x16x32_bf16 v[56:59], v[234:237], v[242:245], v[56:59]
	v_cvt_pk_bf16_f32 v241, v78, v79
	s_waitcnt lgkmcnt(0)
	s_barrier
	ds_read_b128 v[160:163], v201 offset:49152
	ds_read_b128 v[164:167], v209 offset:32768
	ds_read_b128 v[168:171], v202 offset:49152
	ds_read_b128 v[172:175], v209 offset:34816
	ds_read_b128 v[176:179], v203 offset:49152
	ds_read_b128 v[180:183], v209 offset:36864
	ds_read_b128 v[230:233], v246 offset:49152
	v_exp_f32_e32 v88, v88
	v_exp_f32_e32 v92, v92
	v_cvt_pk_bf16_f32 v242, v80, v81
	v_exp_f32_e32 v89, v89
	v_exp_f32_e32 v93, v93
	v_cvt_pk_bf16_f32 v243, v82, v83
	v_exp_f32_e32 v90, v90
	v_exp_f32_e32 v94, v94
	s_waitcnt lgkmcnt(6)
	v_mfma_f32_16x16x32_bf16 v[64:67], v[160:163], v[96:99], 0
	v_cvt_pk_bf16_f32 v204, v84, v85
	v_mfma_f32_16x16x32_bf16 v[68:71], v[160:163], v[112:115], 0
	v_exp_f32_e32 v91, v91
	ds_read_b128 v[234:237], v209 offset:38912
	s_add_u32 s8, s16, 0x3bc00300
	s_addc_u32 s9, s17, 0
	s_add_u32 s6, s15, 0x23a70000
	s_addc_u32 s7, s14, 0
	s_waitcnt lgkmcnt(6)
	v_mfma_f32_16x16x32_bf16 v[0:3], v[164:167], v[216:219], v[0:3]
	v_exp_f32_e32 v95, v95
	v_mfma_f32_16x16x32_bf16 v[4:7], v[164:167], v[238:241], v[4:7]
	v_cvt_pk_bf16_f32 v205, v86, v87
	ds_read_b128 v[160:163], v201 offset:53248
	s_waitcnt vmcnt(4)
	ds_write_b128 v225, v[152:155] offset:16384
	s_waitcnt lgkmcnt(7)
	v_mfma_f32_16x16x32_bf16 v[68:71], v[168:171], v[116:119], v[68:71]
	v_add_f32_e32 v220, v220, v88
	v_mfma_f32_16x16x32_bf16 v[64:67], v[168:171], v[100:103], v[64:67]
	v_add_f32_e32 v221, v221, v92
	ds_read_b128 v[164:167], v209 offset:40960
	ds_write_b128 v226, v[156:159] offset:16384
	s_waitcnt lgkmcnt(8)
	v_mfma_f32_16x16x32_bf16 v[12:15], v[172:175], v[238:241], v[12:15]
	v_add_f32_e32 v220, v220, v89
	v_mfma_f32_16x16x32_bf16 v[8:11], v[172:175], v[216:219], v[8:11]
	v_add_f32_e32 v221, v221, v93
	ds_read_b128 v[168:171], v202 offset:53248
	ds_write_b64 v227, v[132:133] offset:0
	s_waitcnt lgkmcnt(9)
	v_mfma_f32_16x16x32_bf16 v[64:67], v[176:179], v[104:107], v[64:67]
	v_cvt_pk_bf16_f32 v244, v88, v89
	v_mfma_f32_16x16x32_bf16 v[68:71], v[176:179], v[120:123], v[68:71]
	v_cvt_pk_bf16_f32 v245, v90, v91
	ds_read_b128 v[172:175], v209 offset:43008
	ds_write_b64 v228, v[134:135] offset:0
	s_waitcnt lgkmcnt(10)
	v_mfma_f32_16x16x32_bf16 v[16:19], v[180:183], v[216:219], v[16:19]
	v_cvt_pk_bf16_f32 v206, v92, v93
	v_mfma_f32_16x16x32_bf16 v[20:23], v[180:183], v[238:241], v[20:23]
	v_cvt_pk_bf16_f32 v207, v94, v95
	ds_read_b128 v[176:179], v203 offset:53248
	ds_write_b64 v229, v[128:129] offset:0
	s_waitcnt lgkmcnt(11)
	v_mfma_f32_16x16x32_bf16 v[68:71], v[230:233], v[124:127], v[68:71]
	v_mfma_f32_16x16x32_bf16 v[64:67], v[230:233], v[108:111], v[64:67]
	ds_read_b128 v[180:183], v209 offset:45056
	ds_write_b64 v184, v[130:131] offset:0
	s_waitcnt lgkmcnt(12)
	v_mfma_f32_16x16x32_bf16 v[28:31], v[234:237], v[238:241], v[28:31]
	v_mfma_f32_16x16x32_bf16 v[24:27], v[234:237], v[216:219], v[24:27]
	ds_read_b128 v[230:233], v246 offset:53248
	global_load_dwordx4 v[132:135], v198, s[8:9]
	s_waitcnt lgkmcnt(12)
	v_mfma_f32_16x16x32_bf16 v[72:75], v[160:163], v[96:99], 0
	v_add_f32_e32 v220, v220, v90
	v_add_f32_e32 v221, v221, v94
	v_mfma_f32_16x16x32_bf16 v[76:79], v[160:163], v[112:115], 0
	v_add_f32_e32 v220, v220, v91
	v_add_f32_e32 v221, v221, v95
	ds_read_b128 v[234:237], v209 offset:47104
	global_load_dwordx4 v[128:131], v199, s[8:9]
	s_waitcnt lgkmcnt(11)
	v_mfma_f32_16x16x32_bf16 v[32:35], v[164:167], v[216:219], v[32:35]
	v_add_f32_e32 v194, v194, v220
	v_add_f32_e32 v195, v195, v221
	v_mfma_f32_16x16x32_bf16 v[36:39], v[164:167], v[238:241], v[36:39]
	v_exp_f32_e32 v64, v64
	v_exp_f32_e32 v68, v68
	ds_read_b128 v[160:163], v201 offset:57344
	global_load_dwordx4 v[152:155], v196, s[6:7]
	s_waitcnt lgkmcnt(10)
	v_mfma_f32_16x16x32_bf16 v[76:79], v[168:171], v[116:119], v[76:79]
	v_exp_f32_e32 v65, v65
	v_mfma_f32_16x16x32_bf16 v[72:75], v[168:171], v[100:103], v[72:75]
	v_exp_f32_e32 v69, v69
	ds_read_b128 v[164:167], v210 offset:32768
	global_load_dwordx4 v[156:159], v197, s[6:7]
	s_waitcnt lgkmcnt(9)
	v_mfma_f32_16x16x32_bf16 v[44:47], v[172:175], v[238:241], v[44:47]
	v_exp_f32_e32 v66, v66
	v_mfma_f32_16x16x32_bf16 v[40:43], v[172:175], v[216:219], v[40:43]
	v_exp_f32_e32 v70, v70
	ds_read_b128 v[168:171], v202 offset:57344
	s_waitcnt lgkmcnt(8)
	v_mfma_f32_16x16x32_bf16 v[72:75], v[176:179], v[104:107], v[72:75]
	v_exp_f32_e32 v67, v67
	v_mfma_f32_16x16x32_bf16 v[76:79], v[176:179], v[120:123], v[76:79]
	v_exp_f32_e32 v71, v71
	ds_read_b128 v[172:175], v210 offset:34816
	s_waitcnt lgkmcnt(7)
	v_mfma_f32_16x16x32_bf16 v[48:51], v[180:183], v[216:219], v[48:51]
	v_add_f32_e32 v220, v64, v65
	v_mfma_f32_16x16x32_bf16 v[52:55], v[180:183], v[238:241], v[52:55]
	v_add_f32_e32 v221, v68, v69
	ds_read_b128 v[176:179], v203 offset:57344
	s_waitcnt lgkmcnt(6)
	v_mfma_f32_16x16x32_bf16 v[76:79], v[230:233], v[124:127], v[76:79]
	v_add_f32_e32 v220, v220, v66
	v_mfma_f32_16x16x32_bf16 v[72:75], v[230:233], v[108:111], v[72:75]
	v_add_f32_e32 v221, v221, v70
	ds_read_b128 v[180:183], v210 offset:36864
	s_waitcnt lgkmcnt(6)
	v_mfma_f32_16x16x32_bf16 v[60:63], v[234:237], v[238:241], v[60:63]
	v_add_f32_e32 v220, v220, v67
	v_mfma_f32_16x16x32_bf16 v[56:59], v[234:237], v[216:219], v[56:59]
	v_add_f32_e32 v221, v221, v71
	ds_read_b128 v[230:233], v246 offset:57344
	s_waitcnt lgkmcnt(6)
	v_mfma_f32_16x16x32_bf16 v[80:83], v[160:163], v[96:99], 0
	v_exp_f32_e32 v72, v72
	v_exp_f32_e32 v76, v76
	v_mfma_f32_16x16x32_bf16 v[84:87], v[160:163], v[112:115], 0
	v_exp_f32_e32 v73, v73
	v_exp_f32_e32 v77, v77
	ds_read_b128 v[234:237], v210 offset:38912
	s_waitcnt lgkmcnt(6)
	v_mfma_f32_16x16x32_bf16 v[0:3], v[164:167], v[242:245], v[0:3]
	v_exp_f32_e32 v74, v74
	v_exp_f32_e32 v78, v78
	v_mfma_f32_16x16x32_bf16 v[4:7], v[164:167], v[204:207], v[4:7]
	v_exp_f32_e32 v75, v75
	v_exp_f32_e32 v79, v79
	ds_read_b128 v[160:163], v201 offset:61440
	s_waitcnt lgkmcnt(6)
	v_mfma_f32_16x16x32_bf16 v[84:87], v[168:171], v[116:119], v[84:87]
	v_add_f32_e32 v220, v220, v72
	v_mfma_f32_16x16x32_bf16 v[80:83], v[168:171], v[100:103], v[80:83]
	v_add_f32_e32 v221, v221, v76
	ds_read_b128 v[164:167], v210 offset:40960
	s_waitcnt lgkmcnt(6)
	v_mfma_f32_16x16x32_bf16 v[12:15], v[172:175], v[204:207], v[12:15]
	v_add_f32_e32 v220, v220, v73
	v_mfma_f32_16x16x32_bf16 v[8:11], v[172:175], v[242:245], v[8:11]
	v_add_f32_e32 v221, v221, v77
	ds_read_b128 v[168:171], v202 offset:61440
	s_waitcnt lgkmcnt(6)
	v_mfma_f32_16x16x32_bf16 v[80:83], v[176:179], v[104:107], v[80:83]
	v_add_f32_e32 v220, v220, v74
	v_mfma_f32_16x16x32_bf16 v[84:87], v[176:179], v[120:123], v[84:87]
	v_add_f32_e32 v221, v221, v78
	ds_read_b128 v[172:175], v210 offset:43008
	s_waitcnt lgkmcnt(6)
	v_mfma_f32_16x16x32_bf16 v[16:19], v[180:183], v[242:245], v[16:19]
	v_add_f32_e32 v220, v220, v75
	v_mfma_f32_16x16x32_bf16 v[20:23], v[180:183], v[204:207], v[20:23]
	v_add_f32_e32 v221, v221, v79
	ds_read_b128 v[176:179], v203 offset:61440
	s_waitcnt lgkmcnt(6)
	v_mfma_f32_16x16x32_bf16 v[84:87], v[230:233], v[124:127], v[84:87]
	v_cvt_pk_bf16_f32 v216, v64, v65
	v_mfma_f32_16x16x32_bf16 v[80:83], v[230:233], v[108:111], v[80:83]
	v_cvt_pk_bf16_f32 v217, v66, v67
	ds_read_b128 v[180:183], v210 offset:45056
	s_waitcnt lgkmcnt(6)
	v_mfma_f32_16x16x32_bf16 v[28:31], v[234:237], v[204:207], v[28:31]
	v_cvt_pk_bf16_f32 v238, v68, v69
	v_mfma_f32_16x16x32_bf16 v[24:27], v[234:237], v[242:245], v[24:27]
	v_cvt_pk_bf16_f32 v239, v70, v71
	ds_read_b128 v[230:233], v246 offset:61440
	s_waitcnt lgkmcnt(6)
	v_mfma_f32_16x16x32_bf16 v[88:91], v[160:163], v[96:99], 0
	v_exp_f32_e32 v80, v80
	v_exp_f32_e32 v84, v84
	v_mfma_f32_16x16x32_bf16 v[92:95], v[160:163], v[112:115], 0
	v_exp_f32_e32 v81, v81
	v_exp_f32_e32 v85, v85
	ds_read_b128 v[234:237], v210 offset:47104
	s_waitcnt lgkmcnt(6)
	v_mfma_f32_16x16x32_bf16 v[32:35], v[164:167], v[242:245], v[32:35]
	v_exp_f32_e32 v82, v82
	v_exp_f32_e32 v86, v86
	v_mfma_f32_16x16x32_bf16 v[36:39], v[164:167], v[204:207], v[36:39]
	v_exp_f32_e32 v83, v83
	v_exp_f32_e32 v87, v87
	ds_read_b128 v[160:163], v201 offset:0
	s_waitcnt lgkmcnt(6)
	v_mfma_f32_16x16x32_bf16 v[92:95], v[168:171], v[116:119], v[92:95]
	v_add_f32_e32 v220, v220, v80
	v_mfma_f32_16x16x32_bf16 v[88:91], v[168:171], v[100:103], v[88:91]
	v_add_f32_e32 v221, v221, v84
	ds_read_b128 v[164:167], v209 offset:49152
	s_waitcnt lgkmcnt(6)
	v_mfma_f32_16x16x32_bf16 v[44:47], v[172:175], v[204:207], v[44:47]
	v_add_f32_e32 v220, v220, v81
	v_mfma_f32_16x16x32_bf16 v[40:43], v[172:175], v[242:245], v[40:43]
	v_add_f32_e32 v221, v221, v85
	ds_read_b128 v[168:171], v202 offset:0
	s_waitcnt lgkmcnt(6)
	v_mfma_f32_16x16x32_bf16 v[88:91], v[176:179], v[104:107], v[88:91]
	v_add_f32_e32 v220, v220, v82
	v_mfma_f32_16x16x32_bf16 v[92:95], v[176:179], v[120:123], v[92:95]
	v_add_f32_e32 v221, v221, v86
	ds_read_b128 v[172:175], v209 offset:51200
	s_waitcnt lgkmcnt(6)
	v_mfma_f32_16x16x32_bf16 v[48:51], v[180:183], v[242:245], v[48:51]
	v_add_f32_e32 v220, v220, v83
	v_mfma_f32_16x16x32_bf16 v[52:55], v[180:183], v[204:207], v[52:55]
	v_add_f32_e32 v221, v221, v87
	ds_read_b128 v[176:179], v203 offset:0
	s_waitcnt lgkmcnt(6)
	v_mfma_f32_16x16x32_bf16 v[92:95], v[230:233], v[124:127], v[92:95]
	v_cvt_pk_bf16_f32 v218, v72, v73
	v_mfma_f32_16x16x32_bf16 v[88:91], v[230:233], v[108:111], v[88:91]
	v_cvt_pk_bf16_f32 v219, v74, v75
	ds_read_b128 v[180:183], v209 offset:53248
	s_waitcnt lgkmcnt(6)
	v_mfma_f32_16x16x32_bf16 v[60:63], v[234:237], v[204:207], v[60:63]
	v_cvt_pk_bf16_f32 v240, v76, v77
	v_mfma_f32_16x16x32_bf16 v[56:59], v[234:237], v[242:245], v[56:59]
	v_cvt_pk_bf16_f32 v241, v78, v79
	ds_read_b128 v[230:233], v246 offset:0
	s_waitcnt lgkmcnt(6)
	v_mfma_f32_16x16x32_bf16 v[64:67], v[160:163], v[96:99], 0
	v_exp_f32_e32 v88, v88
	v_exp_f32_e32 v92, v92
	v_mfma_f32_16x16x32_bf16 v[68:71], v[160:163], v[112:115], 0
	v_cvt_pk_bf16_f32 v242, v80, v81
	v_exp_f32_e32 v89, v89
	ds_read_b128 v[234:237], v209 offset:55296
	s_add_u32 s8, s16, 0x3bc00380
	s_addc_u32 s9, s17, 0
	s_add_u32 s6, s15, 0x23a80000
	s_addc_u32 s7, s14, 0
	s_waitcnt lgkmcnt(6)
	v_mfma_f32_16x16x32_bf16 v[0:3], v[164:167], v[216:219], v[0:3]
	v_exp_f32_e32 v93, v93
	v_cvt_pk_bf16_f32 v243, v82, v83
	v_mfma_f32_16x16x32_bf16 v[4:7], v[164:167], v[238:241], v[4:7]
	v_exp_f32_e32 v90, v90
	v_exp_f32_e32 v94, v94
	ds_read_b128 v[160:163], v201 offset:4096
	s_waitcnt vmcnt(4)
	ds_write_b128 v225, v[136:139] offset:32768
	s_waitcnt lgkmcnt(7)
	v_mfma_f32_16x16x32_bf16 v[68:71], v[168:171], v[116:119], v[68:71]
	v_cvt_pk_bf16_f32 v204, v84, v85
	v_mfma_f32_16x16x32_bf16 v[64:67], v[168:171], v[100:103], v[64:67]
	v_exp_f32_e32 v91, v91
	ds_read_b128 v[164:167], v209 offset:57344
	ds_write_b128 v226, v[140:143] offset:32768
	s_waitcnt lgkmcnt(8)
	v_mfma_f32_16x16x32_bf16 v[12:15], v[172:175], v[238:241], v[12:15]
	v_exp_f32_e32 v95, v95
	v_mfma_f32_16x16x32_bf16 v[8:11], v[172:175], v[216:219], v[8:11]
	v_cvt_pk_bf16_f32 v205, v86, v87
	ds_read_b128 v[168:171], v202 offset:4096
	ds_write_b64 v227, v[148:149] offset:16384
	s_waitcnt lgkmcnt(9)
	v_mfma_f32_16x16x32_bf16 v[64:67], v[176:179], v[104:107], v[64:67]
	v_add_f32_e32 v220, v220, v88
	v_mfma_f32_16x16x32_bf16 v[68:71], v[176:179], v[120:123], v[68:71]
	v_add_f32_e32 v221, v221, v92
	ds_read_b128 v[172:175], v209 offset:59392
	ds_write_b64 v228, v[150:151] offset:16384
	s_waitcnt lgkmcnt(10)
	v_mfma_f32_16x16x32_bf16 v[16:19], v[180:183], v[216:219], v[16:19]
	v_add_f32_e32 v220, v220, v89
	v_mfma_f32_16x16x32_bf16 v[20:23], v[180:183], v[238:241], v[20:23]
	v_add_f32_e32 v221, v221, v93
	ds_read_b128 v[176:179], v203 offset:4096
	ds_write_b64 v229, v[144:145] offset:16384
	s_waitcnt lgkmcnt(11)
	v_mfma_f32_16x16x32_bf16 v[68:71], v[230:233], v[124:127], v[68:71]
	v_cvt_pk_bf16_f32 v244, v88, v89
	v_mfma_f32_16x16x32_bf16 v[64:67], v[230:233], v[108:111], v[64:67]
	v_cvt_pk_bf16_f32 v245, v90, v91
	ds_read_b128 v[180:183], v209 offset:61440
	ds_write_b64 v184, v[146:147] offset:16384
	s_waitcnt lgkmcnt(12)
	v_mfma_f32_16x16x32_bf16 v[28:31], v[234:237], v[238:241], v[28:31]
	v_cvt_pk_bf16_f32 v206, v92, v93
	v_mfma_f32_16x16x32_bf16 v[24:27], v[234:237], v[216:219], v[24:27]
	v_cvt_pk_bf16_f32 v207, v94, v95
	ds_read_b128 v[230:233], v246 offset:4096
	global_load_dwordx4 v[148:151], v198, s[8:9]
	s_waitcnt lgkmcnt(12)
	v_mfma_f32_16x16x32_bf16 v[72:75], v[160:163], v[96:99], 0
	v_add_f32_e32 v220, v220, v90
	v_add_f32_e32 v221, v221, v94
	v_mfma_f32_16x16x32_bf16 v[76:79], v[160:163], v[112:115], 0
	v_add_f32_e32 v220, v220, v91
	v_add_f32_e32 v221, v221, v95
	ds_read_b128 v[234:237], v209 offset:63488
	global_load_dwordx4 v[144:147], v199, s[8:9]
	s_waitcnt lgkmcnt(11)
	v_mfma_f32_16x16x32_bf16 v[32:35], v[164:167], v[216:219], v[32:35]
	v_add_f32_e32 v194, v194, v220
	v_add_f32_e32 v195, v195, v221
	v_mfma_f32_16x16x32_bf16 v[36:39], v[164:167], v[238:241], v[36:39]
	v_exp_f32_e32 v64, v64
	v_exp_f32_e32 v68, v68
	ds_read_b128 v[160:163], v201 offset:8192
	global_load_dwordx4 v[136:139], v196, s[6:7]
	s_waitcnt lgkmcnt(10)
	v_mfma_f32_16x16x32_bf16 v[76:79], v[168:171], v[116:119], v[76:79]
	v_exp_f32_e32 v65, v65
	v_mfma_f32_16x16x32_bf16 v[72:75], v[168:171], v[100:103], v[72:75]
	v_exp_f32_e32 v69, v69
	ds_read_b128 v[164:167], v210 offset:49152
	global_load_dwordx4 v[140:143], v197, s[6:7]
	s_waitcnt lgkmcnt(9)
	v_mfma_f32_16x16x32_bf16 v[44:47], v[172:175], v[238:241], v[44:47]
	v_exp_f32_e32 v66, v66
	v_mfma_f32_16x16x32_bf16 v[40:43], v[172:175], v[216:219], v[40:43]
	v_exp_f32_e32 v70, v70
	ds_read_b128 v[168:171], v202 offset:8192
	s_waitcnt lgkmcnt(8)
	v_mfma_f32_16x16x32_bf16 v[72:75], v[176:179], v[104:107], v[72:75]
	v_exp_f32_e32 v67, v67
	v_mfma_f32_16x16x32_bf16 v[76:79], v[176:179], v[120:123], v[76:79]
	v_exp_f32_e32 v71, v71
	ds_read_b128 v[172:175], v210 offset:51200
	s_waitcnt lgkmcnt(7)
	v_mfma_f32_16x16x32_bf16 v[48:51], v[180:183], v[216:219], v[48:51]
	v_add_f32_e32 v220, v64, v65
	v_mfma_f32_16x16x32_bf16 v[52:55], v[180:183], v[238:241], v[52:55]
	v_add_f32_e32 v221, v68, v69
	ds_read_b128 v[176:179], v203 offset:8192
	s_waitcnt lgkmcnt(6)
	v_mfma_f32_16x16x32_bf16 v[76:79], v[230:233], v[124:127], v[76:79]
	v_add_f32_e32 v220, v220, v66
	v_mfma_f32_16x16x32_bf16 v[72:75], v[230:233], v[108:111], v[72:75]
	v_add_f32_e32 v221, v221, v70
	ds_read_b128 v[180:183], v210 offset:53248
	s_waitcnt lgkmcnt(6)
	v_mfma_f32_16x16x32_bf16 v[60:63], v[234:237], v[238:241], v[60:63]
	v_add_f32_e32 v220, v220, v67
	v_mfma_f32_16x16x32_bf16 v[56:59], v[234:237], v[216:219], v[56:59]
	v_add_f32_e32 v221, v221, v71
	ds_read_b128 v[230:233], v246 offset:8192
	s_waitcnt lgkmcnt(6)
	v_mfma_f32_16x16x32_bf16 v[80:83], v[160:163], v[96:99], 0
	v_exp_f32_e32 v72, v72
	v_exp_f32_e32 v76, v76
	v_mfma_f32_16x16x32_bf16 v[84:87], v[160:163], v[112:115], 0
	v_exp_f32_e32 v73, v73
	v_exp_f32_e32 v77, v77
	ds_read_b128 v[234:237], v210 offset:55296
	s_waitcnt lgkmcnt(6)
	v_mfma_f32_16x16x32_bf16 v[0:3], v[164:167], v[242:245], v[0:3]
	v_exp_f32_e32 v74, v74
	v_exp_f32_e32 v78, v78
	v_mfma_f32_16x16x32_bf16 v[4:7], v[164:167], v[204:207], v[4:7]
	v_exp_f32_e32 v75, v75
	v_exp_f32_e32 v79, v79
	ds_read_b128 v[160:163], v201 offset:12288
	s_waitcnt lgkmcnt(6)
	v_mfma_f32_16x16x32_bf16 v[84:87], v[168:171], v[116:119], v[84:87]
	v_add_f32_e32 v220, v220, v72
	v_mfma_f32_16x16x32_bf16 v[80:83], v[168:171], v[100:103], v[80:83]
	v_add_f32_e32 v221, v221, v76
	ds_read_b128 v[164:167], v210 offset:57344
	s_waitcnt lgkmcnt(6)
	v_mfma_f32_16x16x32_bf16 v[12:15], v[172:175], v[204:207], v[12:15]
	v_add_f32_e32 v220, v220, v73
	v_mfma_f32_16x16x32_bf16 v[8:11], v[172:175], v[242:245], v[8:11]
	v_add_f32_e32 v221, v221, v77
	ds_read_b128 v[168:171], v202 offset:12288
	s_waitcnt lgkmcnt(6)
	v_mfma_f32_16x16x32_bf16 v[80:83], v[176:179], v[104:107], v[80:83]
	v_add_f32_e32 v220, v220, v74
	v_mfma_f32_16x16x32_bf16 v[84:87], v[176:179], v[120:123], v[84:87]
	v_add_f32_e32 v221, v221, v78
	ds_read_b128 v[172:175], v210 offset:59392
	s_add_u32 s10, s10, 0x200
	s_addc_u32 s11, s11, 0
	s_add_u32 s12, s12, 0x40000
	s_addc_u32 s13, s13, 0
	s_add_i32 s4, s4, 4
	s_cmpk_lt_u32 s4, 0x104
	s_cselect_b64 s[6:7], -1, 0
	s_and_b64 s[6:7], s[0:1], s[6:7]
	s_and_b64 vcc, exec, s[6:7]
	s_waitcnt lgkmcnt(6)
	v_mfma_f32_16x16x32_bf16 v[16:19], v[180:183], v[242:245], v[16:19]
	v_add_f32_e32 v220, v220, v75
	v_mfma_f32_16x16x32_bf16 v[20:23], v[180:183], v[204:207], v[20:23]
	v_add_f32_e32 v221, v221, v79
	ds_read_b128 v[176:179], v203 offset:12288
	s_waitcnt lgkmcnt(6)
	v_mfma_f32_16x16x32_bf16 v[84:87], v[230:233], v[124:127], v[84:87]
	v_cvt_pk_bf16_f32 v216, v64, v65
	v_mfma_f32_16x16x32_bf16 v[80:83], v[230:233], v[108:111], v[80:83]
	v_cvt_pk_bf16_f32 v217, v66, v67
	ds_read_b128 v[180:183], v210 offset:61440
	s_waitcnt lgkmcnt(6)
	v_mfma_f32_16x16x32_bf16 v[28:31], v[234:237], v[204:207], v[28:31]
	v_cvt_pk_bf16_f32 v238, v68, v69
	v_mfma_f32_16x16x32_bf16 v[24:27], v[234:237], v[242:245], v[24:27]
	v_cvt_pk_bf16_f32 v239, v70, v71
	ds_read_b128 v[230:233], v246 offset:12288
	s_waitcnt lgkmcnt(6)
	v_mfma_f32_16x16x32_bf16 v[88:91], v[160:163], v[96:99], 0
	v_exp_f32_e32 v80, v80
	v_exp_f32_e32 v84, v84
	v_mfma_f32_16x16x32_bf16 v[92:95], v[160:163], v[112:115], 0
	v_exp_f32_e32 v81, v81
	v_exp_f32_e32 v85, v85
	ds_read_b128 v[234:237], v210 offset:63488
	s_waitcnt lgkmcnt(6)
	v_mfma_f32_16x16x32_bf16 v[32:35], v[164:167], v[242:245], v[32:35]
	v_exp_f32_e32 v82, v82
	v_exp_f32_e32 v86, v86
	v_mfma_f32_16x16x32_bf16 v[36:39], v[164:167], v[204:207], v[36:39]
	v_exp_f32_e32 v83, v83
	v_exp_f32_e32 v87, v87
	s_waitcnt lgkmcnt(5)
	v_mfma_f32_16x16x32_bf16 v[92:95], v[168:171], v[116:119], v[92:95]
	v_add_f32_e32 v220, v220, v80
	v_mfma_f32_16x16x32_bf16 v[88:91], v[168:171], v[100:103], v[88:91]
	v_add_f32_e32 v221, v221, v84
	s_waitcnt lgkmcnt(4)
	v_mfma_f32_16x16x32_bf16 v[44:47], v[172:175], v[204:207], v[44:47]
	v_add_f32_e32 v220, v220, v81
	v_mfma_f32_16x16x32_bf16 v[40:43], v[172:175], v[242:245], v[40:43]
	v_add_f32_e32 v221, v221, v85
	s_waitcnt lgkmcnt(3)
	v_mfma_f32_16x16x32_bf16 v[88:91], v[176:179], v[104:107], v[88:91]
	v_add_f32_e32 v220, v220, v82
	v_mfma_f32_16x16x32_bf16 v[92:95], v[176:179], v[120:123], v[92:95]
	v_add_f32_e32 v221, v221, v86
	s_waitcnt lgkmcnt(2)
	v_mfma_f32_16x16x32_bf16 v[48:51], v[180:183], v[242:245], v[48:51]
	v_add_f32_e32 v220, v220, v83
	v_mfma_f32_16x16x32_bf16 v[52:55], v[180:183], v[204:207], v[52:55]
	v_add_f32_e32 v221, v221, v87
	s_waitcnt lgkmcnt(1)
	v_mfma_f32_16x16x32_bf16 v[92:95], v[230:233], v[124:127], v[92:95]
	v_cvt_pk_bf16_f32 v218, v72, v73
	v_mfma_f32_16x16x32_bf16 v[88:91], v[230:233], v[108:111], v[88:91]
	v_cvt_pk_bf16_f32 v219, v74, v75
	s_waitcnt lgkmcnt(0)
	v_mfma_f32_16x16x32_bf16 v[60:63], v[234:237], v[204:207], v[60:63]
	v_cvt_pk_bf16_f32 v240, v76, v77
	v_mfma_f32_16x16x32_bf16 v[56:59], v[234:237], v[242:245], v[56:59]
	v_cvt_pk_bf16_f32 v241, v78, v79
	s_cbranch_vccnz .LBB0_734
	s_waitcnt vmcnt(0)
	s_nop 7
	s_nop 7
	ds_swizzle_b32 v64, v194 offset:swizzle(SWAP,16)
	s_waitcnt lgkmcnt(0)
	v_add_f32_e32 v194, v194, v64
	v_mov_b32_e32 v65, v194
	s_nop 1
	v_permlane32_swap_b32_e32 v194, v65
	v_add_f32_e32 v194, v194, v65
	s_nop 0
	v_rcp_f32_e32 v66, v194
	ds_swizzle_b32 v64, v195 offset:swizzle(SWAP,16)
	s_waitcnt lgkmcnt(0)
	v_add_f32_e32 v195, v195, v64
	v_mov_b32_e32 v65, v195
	s_nop 1
	v_permlane32_swap_b32_e32 v195, v65
	v_add_f32_e32 v195, v195, v65
	s_nop 0
	v_rcp_f32_e32 v67, v195
	v_readlane_b32 s100, v250, 8
	v_mbcnt_lo_u32_b32 v68, -1, 0
	v_mbcnt_hi_u32_b32 v68, -1, v68
	v_and_b32_e32 v69, 15, v68
	v_lshrrev_b32_e32 v70, 4, v68
	s_lshr_b32 s101, s100, 1
	v_add_u32_e32 v69, s101, v69
	v_lshlrev_b32_e32 v69, 12, v69
	v_and_b32_e32 v71, 1, v70
	v_lshlrev_b32_e32 v71, 5, v71
	v_and_b32_e32 v70, 2, v70
	v_lshl_add_u32 v71, v70, 3, v71
	v_add_u32_e32 v70, v69, v71
	v_add_u32_e32 v71, 0x10000, v70
	v_mul_f32_e32 v0, v0, v66
	v_mul_f32_e32 v1, v1, v66
	v_mul_f32_e32 v2, v2, v66
	v_mul_f32_e32 v3, v3, v66
	v_mul_f32_e32 v8, v8, v66
	v_mul_f32_e32 v9, v9, v66
	v_mul_f32_e32 v10, v10, v66
	v_mul_f32_e32 v11, v11, v66
	v_cvt_pk_bf16_f32 v72, v0, v1
	v_cvt_pk_bf16_f32 v73, v2, v3
	v_cvt_pk_bf16_f32 v74, v8, v9
	v_cvt_pk_bf16_f32 v75, v10, v11
	s_nop 1
	v_permlane16_swap_b32_e32 v72, v74
	v_permlane16_swap_b32_e32 v73, v75
	s_nop 1
	global_store_dwordx4 v70, v[72:75], s[58:59] offset:0
	v_mul_f32_e32 v16, v16, v66
	v_mul_f32_e32 v17, v17, v66
	v_mul_f32_e32 v18, v18, v66
	v_mul_f32_e32 v19, v19, v66
	v_mul_f32_e32 v24, v24, v66
	v_mul_f32_e32 v25, v25, v66
	v_mul_f32_e32 v26, v26, v66
	v_mul_f32_e32 v27, v27, v66
	v_cvt_pk_bf16_f32 v76, v16, v17
	v_cvt_pk_bf16_f32 v77, v18, v19
	v_cvt_pk_bf16_f32 v78, v24, v25
	v_cvt_pk_bf16_f32 v79, v26, v27
	s_nop 1
	v_permlane16_swap_b32_e32 v76, v78
	v_permlane16_swap_b32_e32 v77, v79
	s_nop 1
	global_store_dwordx4 v70, v[76:79], s[58:59] offset:64
	v_mul_f32_e32 v32, v32, v66
	v_mul_f32_e32 v33, v33, v66
	v_mul_f32_e32 v34, v34, v66
	v_mul_f32_e32 v35, v35, v66
	v_mul_f32_e32 v40, v40, v66
	v_mul_f32_e32 v41, v41, v66
	v_mul_f32_e32 v42, v42, v66
	v_mul_f32_e32 v43, v43, v66
	v_cvt_pk_bf16_f32 v80, v32, v33
	v_cvt_pk_bf16_f32 v81, v34, v35
	v_cvt_pk_bf16_f32 v82, v40, v41
	v_cvt_pk_bf16_f32 v83, v42, v43
	s_nop 1
	v_permlane16_swap_b32_e32 v80, v82
	v_permlane16_swap_b32_e32 v81, v83
	s_nop 1
	global_store_dwordx4 v70, v[80:83], s[58:59] offset:128
	v_mul_f32_e32 v48, v48, v66
	v_mul_f32_e32 v49, v49, v66
	v_mul_f32_e32 v50, v50, v66
	v_mul_f32_e32 v51, v51, v66
	v_mul_f32_e32 v56, v56, v66
	v_mul_f32_e32 v57, v57, v66
	v_mul_f32_e32 v58, v58, v66
	v_mul_f32_e32 v59, v59, v66
	v_cvt_pk_bf16_f32 v84, v48, v49
	v_cvt_pk_bf16_f32 v85, v50, v51
	v_cvt_pk_bf16_f32 v86, v56, v57
	v_cvt_pk_bf16_f32 v87, v58, v59
	s_nop 1
	v_permlane16_swap_b32_e32 v84, v86
	v_permlane16_swap_b32_e32 v85, v87
	s_nop 1
	global_store_dwordx4 v70, v[84:87], s[58:59] offset:192
	v_mul_f32_e32 v4, v4, v67
	v_mul_f32_e32 v5, v5, v67
	v_mul_f32_e32 v6, v6, v67
	v_mul_f32_e32 v7, v7, v67
	v_mul_f32_e32 v12, v12, v67
	v_mul_f32_e32 v13, v13, v67
	v_mul_f32_e32 v14, v14, v67
	v_mul_f32_e32 v15, v15, v67
	v_cvt_pk_bf16_f32 v88, v4, v5
	v_cvt_pk_bf16_f32 v89, v6, v7
	v_cvt_pk_bf16_f32 v90, v12, v13
	v_cvt_pk_bf16_f32 v91, v14, v15
	s_nop 1
	v_permlane16_swap_b32_e32 v88, v90
	v_permlane16_swap_b32_e32 v89, v91
	s_nop 1
	global_store_dwordx4 v71, v[88:91], s[58:59] offset:0
	v_mul_f32_e32 v20, v20, v67
	v_mul_f32_e32 v21, v21, v67
	v_mul_f32_e32 v22, v22, v67
	v_mul_f32_e32 v23, v23, v67
	v_mul_f32_e32 v28, v28, v67
	v_mul_f32_e32 v29, v29, v67
	v_mul_f32_e32 v30, v30, v67
	v_mul_f32_e32 v31, v31, v67
	v_cvt_pk_bf16_f32 v92, v20, v21
	v_cvt_pk_bf16_f32 v93, v22, v23
	v_cvt_pk_bf16_f32 v94, v28, v29
	v_cvt_pk_bf16_f32 v95, v30, v31
	s_nop 1
	v_permlane16_swap_b32_e32 v92, v94
	v_permlane16_swap_b32_e32 v93, v95
	s_nop 1
	global_store_dwordx4 v71, v[92:95], s[58:59] offset:64
	v_mul_f32_e32 v36, v36, v67
	v_mul_f32_e32 v37, v37, v67
	v_mul_f32_e32 v38, v38, v67
	v_mul_f32_e32 v39, v39, v67
	v_mul_f32_e32 v44, v44, v67
	v_mul_f32_e32 v45, v45, v67
	v_mul_f32_e32 v46, v46, v67
	v_mul_f32_e32 v47, v47, v67
	v_cvt_pk_bf16_f32 v72, v36, v37
	v_cvt_pk_bf16_f32 v73, v38, v39
	v_cvt_pk_bf16_f32 v74, v44, v45
	v_cvt_pk_bf16_f32 v75, v46, v47
	s_nop 1
	v_permlane16_swap_b32_e32 v72, v74
	v_permlane16_swap_b32_e32 v73, v75
	s_nop 1
	global_store_dwordx4 v71, v[72:75], s[58:59] offset:128
	v_mul_f32_e32 v52, v52, v67
	v_mul_f32_e32 v53, v53, v67
	v_mul_f32_e32 v54, v54, v67
	v_mul_f32_e32 v55, v55, v67
	v_mul_f32_e32 v60, v60, v67
	v_mul_f32_e32 v61, v61, v67
	v_mul_f32_e32 v62, v62, v67
	v_mul_f32_e32 v63, v63, v67
	v_cvt_pk_bf16_f32 v76, v52, v53
	v_cvt_pk_bf16_f32 v77, v54, v55
	v_cvt_pk_bf16_f32 v78, v60, v61
	v_cvt_pk_bf16_f32 v79, v62, v63
	s_nop 1
	v_permlane16_swap_b32_e32 v76, v78
	v_permlane16_swap_b32_e32 v77, v79
	s_nop 1
	global_store_dwordx4 v71, v[76:79], s[58:59] offset:192
	s_barrier
